# in-projection K loop: LDS-DMA pieces addressed as scalar base + lane offset, 64-bit vector adds removed (on top of v17)
# speedup vs baseline: 1.0044x; 1.0044x over previous
.LBB0_301:
	s_waitcnt vmcnt(6)
	ds_read_b128 v[106:109], v213
	ds_read_b128 v[110:113], v213 offset:1024
	ds_read_b128 v[126:129], v213 offset:2048
	ds_read_b128 v[130:133], v213 offset:3072
	s_add_u32 s68, s66, 0xfff80080
	s_addc_u32 s69, s67, -1
	s_cmp_eq_u32 s94, 28
	s_cselect_b32 s71, s11, s69
	s_cselect_b32 s70, s16, s68
	s_cselect_b32 s69, s57, s93
	s_cselect_b32 s68, s59, s92
	s_add_i32 m0, s65, 0xc000
	ds_read_b128 v[146:149], v214
	ds_read_b128 v[178:181], v214 offset:1024
	ds_read_b128 v[182:185], v214 offset:2048
	ds_read_b128 v[186:189], v214 offset:3072
	ds_read_b128 v[190:193], v214 offset:4096
	ds_read_b128 v[194:197], v214 offset:5120
	ds_read_b128 v[198:201], v214 offset:6144
	ds_read_b128 v[220:223], v214 offset:7168
	global_load_lds_dwordx4 v170, s[66:67]
	s_add_i32 m0, s65, 0xe000
	s_nop 0
	global_load_lds_dwordx4 v172, s[66:67]
	s_waitcnt lgkmcnt(8)
	s_barrier
	s_waitcnt lgkmcnt(0)
	s_setprio 1
	s_waitcnt lgkmcnt(0)
	v_mfma_i32_16x16x64_i8 v[142:145], v[106:109], v[146:149], v[142:145]
	v_mfma_i32_16x16x64_i8 v[138:141], v[126:129], v[146:149], v[138:141]
	v_mfma_i32_16x16x64_i8 v[118:121], v[106:109], v[182:185], v[118:121]
	v_mfma_i32_16x16x64_i8 v[114:117], v[126:129], v[182:185], v[114:117]
	v_mfma_i32_16x16x64_i8 v[94:97], v[106:109], v[190:193], v[94:97]
	v_mfma_i32_16x16x64_i8 v[90:93], v[126:129], v[190:193], v[90:93]
	v_mfma_i32_16x16x64_i8 v[78:81], v[106:109], v[198:201], v[78:81]
	v_mfma_i32_16x16x64_i8 v[74:77], v[126:129], v[198:201], v[74:77]
	v_mfma_i32_16x16x64_i8 v[142:145], v[110:113], v[178:181], v[142:145]
	v_mfma_i32_16x16x64_i8 v[138:141], v[130:133], v[178:181], v[138:141]
	v_mfma_i32_16x16x64_i8 v[118:121], v[110:113], v[186:189], v[118:121]
	v_mfma_i32_16x16x64_i8 v[114:117], v[130:133], v[186:189], v[114:117]
	v_mfma_i32_16x16x64_i8 v[94:97], v[110:113], v[194:197], v[94:97]
	v_mfma_i32_16x16x64_i8 v[90:93], v[130:133], v[194:197], v[90:93]
	v_mfma_i32_16x16x64_i8 v[78:81], v[110:113], v[220:223], v[78:81]
	v_mfma_i32_16x16x64_i8 v[74:77], v[130:133], v[220:223], v[74:77]
	s_setprio 0
	s_barrier
	s_add_i32 s95, s89, s75
	s_mov_b32 m0, s95
	ds_read_b128 v[224:227], v215
	ds_read_b128 v[228:231], v215 offset:1024
	ds_read_b128 v[232:235], v215 offset:2048
	ds_read_b128 v[236:239], v215 offset:3072
	global_load_lds_dwordx4 v152, s[68:69]
	s_add_i32 m0, s95, 0x2000
	s_nop 0
	global_load_lds_dwordx4 v156, s[68:69]
	s_barrier
	s_waitcnt lgkmcnt(0)
	s_setprio 1
	s_waitcnt lgkmcnt(0)
	v_mfma_i32_16x16x64_i8 v[134:137], v[224:227], v[146:149], v[134:137]
	v_mfma_i32_16x16x64_i8 v[122:125], v[232:235], v[146:149], v[122:125]
	v_mfma_i32_16x16x64_i8 v[102:105], v[224:227], v[182:185], v[102:105]
	v_mfma_i32_16x16x64_i8 v[98:101], v[232:235], v[182:185], v[98:101]
	v_mfma_i32_16x16x64_i8 v[86:89], v[224:227], v[190:193], v[86:89]
	v_mfma_i32_16x16x64_i8 v[82:85], v[232:235], v[190:193], v[82:85]
	v_mfma_i32_16x16x64_i8 v[70:73], v[224:227], v[198:201], v[70:73]
	v_mfma_i32_16x16x64_i8 v[66:69], v[232:235], v[198:201], v[66:69]
	v_mfma_i32_16x16x64_i8 v[134:137], v[228:231], v[178:181], v[134:137]
	v_mfma_i32_16x16x64_i8 v[122:125], v[236:239], v[178:181], v[122:125]
	v_mfma_i32_16x16x64_i8 v[102:105], v[228:231], v[186:189], v[102:105]
	v_mfma_i32_16x16x64_i8 v[98:101], v[236:239], v[186:189], v[98:101]
	v_mfma_i32_16x16x64_i8 v[86:89], v[228:231], v[194:197], v[86:89]
	v_mfma_i32_16x16x64_i8 v[82:85], v[236:239], v[194:197], v[82:85]
	v_mfma_i32_16x16x64_i8 v[70:73], v[228:231], v[220:223], v[70:73]
	v_mfma_i32_16x16x64_i8 v[66:69], v[236:239], v[220:223], v[66:69]
	s_setprio 0
	s_mov_b32 m0, s65
	s_add_u32 s98, s70, 0x80
	s_addc_u32 s99, s71, 0
	s_barrier
	ds_read_b128 v[146:149], v214 offset:16384
	ds_read_b128 v[178:181], v214 offset:17408
	ds_read_b128 v[182:185], v214 offset:18432
	ds_read_b128 v[186:189], v214 offset:19456
	ds_read_b128 v[190:193], v214 offset:20480
	ds_read_b128 v[194:197], v214 offset:21504
	ds_read_b128 v[198:201], v214 offset:22528
	ds_read_b128 v[220:223], v214 offset:23552
	global_load_lds_dwordx4 v150, s[70:71]
	s_mov_b32 m0, s76
	s_nop 0
	global_load_lds_dwordx4 v154, s[70:71]
	s_barrier
	s_waitcnt lgkmcnt(0)
	s_setprio 1
	s_waitcnt lgkmcnt(0)
	v_mfma_i32_16x16x64_i8 v[62:65], v[106:109], v[146:149], v[62:65]
	v_mfma_i32_16x16x64_i8 v[58:61], v[126:129], v[146:149], v[58:61]
	v_mfma_i32_16x16x64_i8 v[46:49], v[106:109], v[182:185], v[46:49]
	v_mfma_i32_16x16x64_i8 v[42:45], v[126:129], v[182:185], v[42:45]
	v_mfma_i32_16x16x64_i8 v[30:33], v[106:109], v[190:193], v[30:33]
	v_mfma_i32_16x16x64_i8 v[26:29], v[126:129], v[190:193], v[26:29]
	v_mfma_i32_16x16x64_i8 v[14:17], v[106:109], v[198:201], v[14:17]
	v_mfma_i32_16x16x64_i8 v[10:13], v[126:129], v[198:201], v[10:13]
	v_mfma_i32_16x16x64_i8 v[62:65], v[110:113], v[178:181], v[62:65]
	v_mfma_i32_16x16x64_i8 v[58:61], v[130:133], v[178:181], v[58:61]
	v_mfma_i32_16x16x64_i8 v[46:49], v[110:113], v[186:189], v[46:49]
	v_mfma_i32_16x16x64_i8 v[42:45], v[130:133], v[186:189], v[42:45]
	v_mfma_i32_16x16x64_i8 v[30:33], v[110:113], v[194:197], v[30:33]
	v_mfma_i32_16x16x64_i8 v[26:29], v[130:133], v[194:197], v[26:29]
	v_mfma_i32_16x16x64_i8 v[14:17], v[110:113], v[220:223], v[14:17]
	v_mfma_i32_16x16x64_i8 v[10:13], v[130:133], v[220:223], v[10:13]
	s_setprio 0
	s_barrier
	s_add_u32 s96, s68, 0x80000
	s_addc_u32 s97, s69, 0
	s_add_i32 s95, s90, s75
	s_mov_b32 m0, s95
	s_nop 0
	global_load_lds_dwordx4 v152, s[96:97]
	s_add_i32 m0, s95, 0x2000
	s_nop 0
	global_load_lds_dwordx4 v156, s[96:97]
	s_waitcnt vmcnt(6)
	s_barrier
	s_setprio 1
	v_mfma_i32_16x16x64_i8 v[54:57], v[224:227], v[146:149], v[54:57]
	v_mfma_i32_16x16x64_i8 v[50:53], v[232:235], v[146:149], v[50:53]
	v_mfma_i32_16x16x64_i8 v[38:41], v[224:227], v[182:185], v[38:41]
	v_mfma_i32_16x16x64_i8 v[34:37], v[232:235], v[182:185], v[34:37]
	v_mfma_i32_16x16x64_i8 v[22:25], v[224:227], v[190:193], v[22:25]
	v_mfma_i32_16x16x64_i8 v[18:21], v[232:235], v[190:193], v[18:21]
	v_mfma_i32_16x16x64_i8 v[6:9], v[224:227], v[198:201], v[6:9]
	v_mfma_i32_16x16x64_i8 v[2:5], v[232:235], v[198:201], v[2:5]
	v_mfma_i32_16x16x64_i8 v[54:57], v[228:231], v[178:181], v[54:57]
	v_mfma_i32_16x16x64_i8 v[50:53], v[236:239], v[178:181], v[50:53]
	v_mfma_i32_16x16x64_i8 v[38:41], v[228:231], v[186:189], v[38:41]
	v_mfma_i32_16x16x64_i8 v[34:37], v[236:239], v[186:189], v[34:37]
	v_mfma_i32_16x16x64_i8 v[22:25], v[228:231], v[194:197], v[22:25]
	v_mfma_i32_16x16x64_i8 v[18:21], v[236:239], v[194:197], v[18:21]
	v_mfma_i32_16x16x64_i8 v[6:9], v[228:231], v[220:223], v[6:9]
	v_mfma_i32_16x16x64_i8 v[2:5], v[236:239], v[220:223], v[2:5]
	s_setprio 0
	s_add_i32 s95, 0, 0x18000
	v_add_u32_e32 v130, s95, v163
	s_barrier
	ds_read_b128 v[106:109], v130
	ds_read_b128 v[110:113], v130 offset:1024
	ds_read_b128 v[126:129], v130 offset:2048
	ds_read_b128 v[130:133], v130 offset:3072
	s_add_u32 s70, s70, 0x80000
	s_addc_u32 s71, s71, 0
	s_mov_b32 m0, s77
	ds_read_b128 v[146:149], v214 offset:32768
	ds_read_b128 v[178:181], v214 offset:33792
	ds_read_b128 v[182:185], v214 offset:34816
	ds_read_b128 v[186:189], v214 offset:35840
	ds_read_b128 v[190:193], v214 offset:36864
	ds_read_b128 v[194:197], v214 offset:37888
	ds_read_b128 v[198:201], v214 offset:38912
	ds_read_b128 v[220:223], v214 offset:39936
	global_load_lds_dwordx4 v150, s[70:71]
	s_mov_b32 m0, s78
	s_nop 0
	global_load_lds_dwordx4 v154, s[70:71]
	s_waitcnt lgkmcnt(8)
	s_barrier
	s_waitcnt lgkmcnt(0)
	s_setprio 1
	s_waitcnt lgkmcnt(0)
	v_mfma_i32_16x16x64_i8 v[142:145], v[106:109], v[146:149], v[142:145]
	v_mfma_i32_16x16x64_i8 v[138:141], v[126:129], v[146:149], v[138:141]
	v_mfma_i32_16x16x64_i8 v[118:121], v[106:109], v[182:185], v[118:121]
	v_mfma_i32_16x16x64_i8 v[114:117], v[126:129], v[182:185], v[114:117]
	v_mfma_i32_16x16x64_i8 v[94:97], v[106:109], v[190:193], v[94:97]
	v_mfma_i32_16x16x64_i8 v[90:93], v[126:129], v[190:193], v[90:93]
	v_mfma_i32_16x16x64_i8 v[78:81], v[106:109], v[198:201], v[78:81]
	v_mfma_i32_16x16x64_i8 v[74:77], v[126:129], v[198:201], v[74:77]
	v_mfma_i32_16x16x64_i8 v[142:145], v[110:113], v[178:181], v[142:145]
	v_mfma_i32_16x16x64_i8 v[138:141], v[130:133], v[178:181], v[138:141]
	v_mfma_i32_16x16x64_i8 v[118:121], v[110:113], v[186:189], v[118:121]
	v_mfma_i32_16x16x64_i8 v[114:117], v[130:133], v[186:189], v[114:117]
	v_mfma_i32_16x16x64_i8 v[94:97], v[110:113], v[194:197], v[94:97]
	v_mfma_i32_16x16x64_i8 v[90:93], v[130:133], v[194:197], v[90:93]
	v_mfma_i32_16x16x64_i8 v[78:81], v[110:113], v[220:223], v[78:81]
	v_mfma_i32_16x16x64_i8 v[74:77], v[130:133], v[220:223], v[74:77]
	s_setprio 0
	s_barrier
	s_add_i32 s70, 0, 0x1c000
	s_add_i32 s71, s95, s75
	v_add_u32_e32 v158, s70, v163
	s_add_u32 s100, s68, 0x80
	s_addc_u32 s101, s69, 0
	s_mov_b32 m0, s71
	ds_read_b128 v[224:227], v158
	ds_read_b128 v[228:231], v158 offset:1024
	ds_read_b128 v[232:235], v158 offset:2048
	ds_read_b128 v[236:239], v158 offset:3072
	global_load_lds_dwordx4 v152, s[100:101]
	s_add_i32 m0, s71, 0x2000
	s_nop 0
	global_load_lds_dwordx4 v156, s[100:101]
	s_barrier
	s_waitcnt lgkmcnt(0)
	s_setprio 1
	s_waitcnt lgkmcnt(0)
	v_mfma_i32_16x16x64_i8 v[134:137], v[224:227], v[146:149], v[134:137]
	v_mfma_i32_16x16x64_i8 v[122:125], v[232:235], v[146:149], v[122:125]
	v_mfma_i32_16x16x64_i8 v[102:105], v[224:227], v[182:185], v[102:105]
	v_mfma_i32_16x16x64_i8 v[98:101], v[232:235], v[182:185], v[98:101]
	v_mfma_i32_16x16x64_i8 v[86:89], v[224:227], v[190:193], v[86:89]
	v_mfma_i32_16x16x64_i8 v[82:85], v[232:235], v[190:193], v[82:85]
	v_mfma_i32_16x16x64_i8 v[70:73], v[224:227], v[198:201], v[70:73]
	v_mfma_i32_16x16x64_i8 v[66:69], v[232:235], v[198:201], v[66:69]
	v_mfma_i32_16x16x64_i8 v[134:137], v[228:231], v[178:181], v[134:137]
	v_mfma_i32_16x16x64_i8 v[122:125], v[236:239], v[178:181], v[122:125]
	v_mfma_i32_16x16x64_i8 v[102:105], v[228:231], v[186:189], v[102:105]
	v_mfma_i32_16x16x64_i8 v[98:101], v[236:239], v[186:189], v[98:101]
	v_mfma_i32_16x16x64_i8 v[86:89], v[228:231], v[194:197], v[86:89]
	v_mfma_i32_16x16x64_i8 v[82:85], v[236:239], v[194:197], v[82:85]
	v_mfma_i32_16x16x64_i8 v[70:73], v[228:231], v[220:223], v[70:73]
	v_mfma_i32_16x16x64_i8 v[66:69], v[236:239], v[220:223], v[66:69]
	s_setprio 0
	s_mov_b32 m0, s85
	s_barrier
	ds_read_b128 v[146:149], v214 offset:49152
	ds_read_b128 v[178:181], v214 offset:50176
	ds_read_b128 v[182:185], v214 offset:51200
	ds_read_b128 v[186:189], v214 offset:52224
	ds_read_b128 v[190:193], v214 offset:53248
	ds_read_b128 v[194:197], v214 offset:54272
	ds_read_b128 v[198:201], v214 offset:55296
	ds_read_b128 v[220:223], v214 offset:56320
	global_load_lds_dwordx4 v150, s[98:99]
	s_mov_b32 m0, s86
	s_nop 0
	global_load_lds_dwordx4 v154, s[98:99]
	s_barrier
	s_waitcnt lgkmcnt(0)
	s_setprio 1
	s_waitcnt lgkmcnt(0)
	v_mfma_i32_16x16x64_i8 v[62:65], v[106:109], v[146:149], v[62:65]
	v_mfma_i32_16x16x64_i8 v[58:61], v[126:129], v[146:149], v[58:61]
	v_mfma_i32_16x16x64_i8 v[46:49], v[106:109], v[182:185], v[46:49]
	v_mfma_i32_16x16x64_i8 v[42:45], v[126:129], v[182:185], v[42:45]
	v_mfma_i32_16x16x64_i8 v[30:33], v[106:109], v[190:193], v[30:33]
	v_mfma_i32_16x16x64_i8 v[26:29], v[126:129], v[190:193], v[26:29]
	v_mfma_i32_16x16x64_i8 v[14:17], v[106:109], v[198:201], v[14:17]
	v_mfma_i32_16x16x64_i8 v[10:13], v[126:129], v[198:201], v[10:13]
	v_mfma_i32_16x16x64_i8 v[62:65], v[110:113], v[178:181], v[62:65]
	v_mfma_i32_16x16x64_i8 v[58:61], v[130:133], v[178:181], v[58:61]
	v_mfma_i32_16x16x64_i8 v[46:49], v[110:113], v[186:189], v[46:49]
	v_mfma_i32_16x16x64_i8 v[42:45], v[130:133], v[186:189], v[42:45]
	v_mfma_i32_16x16x64_i8 v[30:33], v[110:113], v[194:197], v[30:33]
	v_mfma_i32_16x16x64_i8 v[26:29], v[130:133], v[194:197], v[26:29]
	v_mfma_i32_16x16x64_i8 v[14:17], v[110:113], v[220:223], v[14:17]
	v_mfma_i32_16x16x64_i8 v[10:13], v[130:133], v[220:223], v[10:13]
	s_setprio 0
	s_barrier
	s_add_u32 s68, s68, 0x80080
	s_addc_u32 s69, s69, 0
	s_add_i32 s70, s70, s75
	s_mov_b32 m0, s70
	s_nop 0
	global_load_lds_dwordx4 v152, s[68:69]
	s_add_i32 m0, s70, 0x2000
	s_nop 0
	global_load_lds_dwordx4 v156, s[68:69]
	s_waitcnt vmcnt(6)
	s_barrier
	s_setprio 1
	v_mfma_i32_16x16x64_i8 v[54:57], v[224:227], v[146:149], v[54:57]
	v_mfma_i32_16x16x64_i8 v[50:53], v[232:235], v[146:149], v[50:53]
	v_mfma_i32_16x16x64_i8 v[38:41], v[224:227], v[182:185], v[38:41]
	v_mfma_i32_16x16x64_i8 v[34:37], v[232:235], v[182:185], v[34:37]
	v_mfma_i32_16x16x64_i8 v[22:25], v[224:227], v[190:193], v[22:25]
	v_mfma_i32_16x16x64_i8 v[18:21], v[232:235], v[190:193], v[18:21]
	v_mfma_i32_16x16x64_i8 v[6:9], v[224:227], v[198:201], v[6:9]
	v_mfma_i32_16x16x64_i8 v[2:5], v[232:235], v[198:201], v[2:5]
	v_mfma_i32_16x16x64_i8 v[54:57], v[228:231], v[178:181], v[54:57]
	v_mfma_i32_16x16x64_i8 v[50:53], v[236:239], v[178:181], v[50:53]
	v_mfma_i32_16x16x64_i8 v[38:41], v[228:231], v[186:189], v[38:41]
	v_mfma_i32_16x16x64_i8 v[34:37], v[236:239], v[186:189], v[34:37]
	v_mfma_i32_16x16x64_i8 v[22:25], v[228:231], v[194:197], v[22:25]
	v_mfma_i32_16x16x64_i8 v[18:21], v[236:239], v[194:197], v[18:21]
	v_mfma_i32_16x16x64_i8 v[6:9], v[228:231], v[220:223], v[6:9]
	v_mfma_i32_16x16x64_i8 v[2:5], v[236:239], v[220:223], v[2:5]
	s_setprio 0
	s_add_i32 s94, s94, 2
	s_add_u32 s66, s66, 0x100
	s_addc_u32 s67, s67, 0
	s_add_u32 s92, s92, 0x100
	s_addc_u32 s93, s93, 0
	s_cmp_gt_u32 s94, 29
	s_barrier
	s_cbranch_scc0 .LBB0_301
	s_and_b64 vcc, exec, s[36:37]
	s_cbranch_vccz .LBB0_304
	s_barrier
